# removed the redundant vmcnt waits at the K-loop heads of the w_in and down-projection GEMMs (buffers read there are already guaranteed by the previous phase's counted wait + barrier, as in the other G
# speedup vs baseline: 1.0282x; 1.0115x over previous
; #define PG8_STAGE(bufoff, gbase, voff) do { _Pragma("unroll") for (int _i = 0; _i < 2; ++_i) \
;         __builtin_amdgcn_raw_ptr_buffer_load_lds(rsrc, (LAS void*)(lds + (bufoff) + ldsw + _i * 8192), 16, (int)(voff)[_i], (int)(gbase), 0, 0); } while (0)
; #define PG8_STAGE_A(bufoff, h, goff) do { if constexpr (GATHER) { PG8_STAGE(bufoff, goff, vG[h]); } else { PG8_STAGE(bufoff, (goff) + (h) * hstep, voffA); } } while (0)
; #define PG8_WAIT_V(n) asm volatile("s_waitcnt vmcnt(" #n ")" ::: "memory")
; #define PG8_WAIT_L(n) asm volatile("s_waitcnt lgkmcnt(" #n ")" ::: "memory")
; #define PG8_BAR __builtin_amdgcn_s_barrier()
; #define PG8_SCHED __builtin_amdgcn_sched_barrier(0)
;     DI int row_cnt(const pg8::Unit& u) const { return __builtin_amdgcn_readfirstlane(tab[u.a0]) - u.ldc; }
;     ...
;             PG8_LDB(B0, 0, 0); PG8_LDB(B1, 0, 1); PG8_SCHED; PG8_LDA(At, 0, 0); PG8_STAGE_A(PG8_SA(1, 1), 1, a1);
;             if constexpr (GATHER) { if (last && has_next) load_rows((ui + 1) & 1, S.row_cnt(nxt)); }
;             PG8_WAIT_V(8); PG8_WAIT_L(0); PG8_BAR; PG8_MMA(0, 0, At, B0); PG8_MMA(0, 1, At, B1); PG8_BAR; PG8_SCHED;
;             PG8_LDA(At, 0, 1); PG8_STAGE(PG8_SB(0, 0), b2, voffB); PG8_STAGE(PG8_SB(0, 1), b2 + hstep, voffB); PG8_STAGE_A(PG8_SA(0, 0), 0, a2);
;             PG8_WAIT_V(8); PG8_WAIT_L(0); PG8_BAR; PG8_MMA(1, 0, At, B0); PG8_MMA(1, 1, At, B1); PG8_BAR; PG8_SCHED;
.LBB0_337:
	ds_read_b128 v[64:67], v159
	ds_read_b128 v[68:71], v160
	ds_read_b128 v[72:75], v161
	ds_read_b128 v[76:79], v162
	ds_read_b128 v[144:147], v163
	ds_read_b128 v[148:151], v164
	ds_read_b128 v[174:177], v165
	ds_read_b128 v[178:181], v166
	s_add_i32 s4, s2, 0xfffc0080
	s_cmp_eq_u32 s10, 12
	s_cselect_b32 s53, s41, s4
	s_cselect_b32 s51, s82, s3
	s_add_i32 s50, s53, 0x80
	s_mov_b32 s4, s86
	s_mov_b32 m0, s74
	ds_read_b128 v[182:185], v167
	ds_read_b128 v[186:189], v167 offset:2048
	ds_read_b128 v[190:193], v168
	ds_read_b128 v[194:197], v168 offset:2048
	ds_read_b128 v[198:201], v167 offset:4096
	ds_read_b128 v[202:205], v167 offset:6144
	ds_read_b128 v[206:209], v168 offset:4096
	ds_read_b128 v[210:213], v168 offset:6144
	buffer_load_dwordx4 v153, s[4:7], s2 offen lds
	s_mov_b32 m0, s77
	s_nop 0
	buffer_load_dwordx4 v155, s[4:7], s2 offen lds
	s_waitcnt vmcnt(8)
	s_waitcnt lgkmcnt(0)
	s_barrier
	s_setprio 1
	s_waitcnt lgkmcnt(7)
	v_mfma_i32_16x16x64_i8 v[60:63], v[64:67], v[182:185], v[60:63]
	v_mfma_i32_16x16x64_i8 v[56:59], v[72:75], v[182:185], v[56:59]
	s_waitcnt lgkmcnt(6)
	v_mfma_i32_16x16x64_i8 v[52:55], v[64:67], v[186:189], v[52:55]
	v_mfma_i32_16x16x64_i8 v[48:51], v[72:75], v[186:189], v[48:51]
	s_waitcnt lgkmcnt(3)
	v_mfma_i32_16x16x64_i8 v[44:47], v[64:67], v[198:201], v[44:47]
	v_mfma_i32_16x16x64_i8 v[40:43], v[72:75], v[198:201], v[40:43]
	s_waitcnt lgkmcnt(2)
	v_mfma_i32_16x16x64_i8 v[36:39], v[64:67], v[202:205], v[36:39]
	v_mfma_i32_16x16x64_i8 v[32:35], v[72:75], v[202:205], v[32:35]
	v_mfma_i32_16x16x64_i8 v[60:63], v[68:71], v[190:193], v[60:63]
	v_mfma_i32_16x16x64_i8 v[56:59], v[76:79], v[190:193], v[56:59]
	v_mfma_i32_16x16x64_i8 v[52:55], v[68:71], v[194:197], v[52:55]
	v_mfma_i32_16x16x64_i8 v[48:51], v[76:79], v[194:197], v[48:51]
	s_waitcnt lgkmcnt(1)
	v_mfma_i32_16x16x64_i8 v[44:47], v[68:71], v[206:209], v[44:47]
	v_mfma_i32_16x16x64_i8 v[40:43], v[76:79], v[206:209], v[40:43]
	s_waitcnt lgkmcnt(0)
	v_mfma_i32_16x16x64_i8 v[36:39], v[68:71], v[210:213], v[36:39]
	v_mfma_i32_16x16x64_i8 v[32:35], v[76:79], v[210:213], v[32:35]
	s_setprio 0
	s_setprio 1
	v_mfma_i32_16x16x64_i8 v[140:143], v[144:147], v[182:185], v[140:143]
	v_mfma_i32_16x16x64_i8 v[136:139], v[174:177], v[182:185], v[136:139]
	v_mfma_i32_16x16x64_i8 v[132:135], v[144:147], v[186:189], v[132:135]
	v_mfma_i32_16x16x64_i8 v[128:131], v[174:177], v[186:189], v[128:131]
	v_mfma_i32_16x16x64_i8 v[124:127], v[144:147], v[198:201], v[124:127]
	v_mfma_i32_16x16x64_i8 v[120:123], v[174:177], v[198:201], v[120:123]
	v_mfma_i32_16x16x64_i8 v[116:119], v[144:147], v[202:205], v[116:119]
	v_mfma_i32_16x16x64_i8 v[112:115], v[174:177], v[202:205], v[112:115]
	v_mfma_i32_16x16x64_i8 v[140:143], v[148:151], v[190:193], v[140:143]
	v_mfma_i32_16x16x64_i8 v[136:139], v[178:181], v[190:193], v[136:139]
	v_mfma_i32_16x16x64_i8 v[132:135], v[148:151], v[194:197], v[132:135]
	v_mfma_i32_16x16x64_i8 v[128:131], v[178:181], v[194:197], v[128:131]
	v_mfma_i32_16x16x64_i8 v[124:127], v[148:151], v[206:209], v[124:127]
	v_mfma_i32_16x16x64_i8 v[120:123], v[178:181], v[206:209], v[120:123]
	v_mfma_i32_16x16x64_i8 v[116:119], v[148:151], v[210:213], v[116:119]
	v_mfma_i32_16x16x64_i8 v[112:115], v[178:181], v[210:213], v[112:115]
	s_setprio 0
	s_barrier
	s_mov_b32 m0, s57
	ds_read_b128 v[182:185], v167 offset:16384
	ds_read_b128 v[186:189], v167 offset:18432
	ds_read_b128 v[190:193], v168 offset:16384
	ds_read_b128 v[194:197], v168 offset:18432
	ds_read_b128 v[198:201], v167 offset:20480
	ds_read_b128 v[202:205], v167 offset:22528
	ds_read_b128 v[206:209], v168 offset:20480
	ds_read_b128 v[210:213], v168 offset:22528
	buffer_load_dwordx4 v154, s[4:7], s51 offen lds
	s_mov_b32 m0, s58
	s_add_i32 s54, s51, 0x40000
	buffer_load_dwordx4 v156, s[4:7], s51 offen lds
	s_mov_b32 m0, s59
	s_nop 0
	buffer_load_dwordx4 v154, s[4:7], s54 offen lds
	s_mov_b32 m0, s60
	s_nop 0
	buffer_load_dwordx4 v156, s[4:7], s54 offen lds
	s_mov_b32 m0, s56
	s_nop 0
	buffer_load_dwordx4 v153, s[4:7], s53 offen lds
	s_mov_b32 m0, s61
	s_nop 0
	buffer_load_dwordx4 v155, s[4:7], s53 offen lds
	s_waitcnt vmcnt(8)
	s_waitcnt lgkmcnt(0)
	s_barrier
	s_setprio 1
	s_waitcnt lgkmcnt(7)
	v_mfma_i32_16x16x64_i8 v[28:31], v[64:67], v[182:185], v[28:31]
	v_mfma_i32_16x16x64_i8 v[24:27], v[72:75], v[182:185], v[24:27]
	s_waitcnt lgkmcnt(6)
	v_mfma_i32_16x16x64_i8 v[20:23], v[64:67], v[186:189], v[20:23]
	v_mfma_i32_16x16x64_i8 v[16:19], v[72:75], v[186:189], v[16:19]
	s_waitcnt lgkmcnt(3)
	v_mfma_i32_16x16x64_i8 v[12:15], v[64:67], v[198:201], v[12:15]
	v_mfma_i32_16x16x64_i8 v[8:11], v[72:75], v[198:201], v[8:11]
	s_waitcnt lgkmcnt(2)
	v_mfma_i32_16x16x64_i8 v[4:7], v[64:67], v[202:205], v[4:7]
	v_mfma_i32_16x16x64_i8 v[0:3], v[72:75], v[202:205], v[0:3]
	v_mfma_i32_16x16x64_i8 v[28:31], v[68:71], v[190:193], v[28:31]
	v_mfma_i32_16x16x64_i8 v[24:27], v[76:79], v[190:193], v[24:27]
	v_mfma_i32_16x16x64_i8 v[20:23], v[68:71], v[194:197], v[20:23]
	v_mfma_i32_16x16x64_i8 v[16:19], v[76:79], v[194:197], v[16:19]
	s_waitcnt lgkmcnt(1)
	v_mfma_i32_16x16x64_i8 v[12:15], v[68:71], v[206:209], v[12:15]
	v_mfma_i32_16x16x64_i8 v[8:11], v[76:79], v[206:209], v[8:11]
	s_waitcnt lgkmcnt(0)
	v_mfma_i32_16x16x64_i8 v[4:7], v[68:71], v[210:213], v[4:7]
	v_mfma_i32_16x16x64_i8 v[0:3], v[76:79], v[210:213], v[0:3]
	s_setprio 0
	s_setprio 1
	v_mfma_i32_16x16x64_i8 v[92:95], v[144:147], v[198:201], v[92:95]
	v_mfma_i32_16x16x64_i8 v[88:91], v[174:177], v[198:201], v[88:91]
	v_mfma_i32_16x16x64_i8 v[84:87], v[144:147], v[202:205], v[84:87]
	v_mfma_i32_16x16x64_i8 v[80:83], v[174:177], v[202:205], v[80:83]
	v_mfma_i32_16x16x64_i8 v[64:67], v[144:147], v[182:185], v[108:111]
	v_mfma_i32_16x16x64_i8 v[68:71], v[174:177], v[182:185], v[104:107]
	v_mfma_i32_16x16x64_i8 v[72:75], v[144:147], v[186:189], v[100:103]
	v_mfma_i32_16x16x64_i8 v[76:79], v[174:177], v[186:189], v[96:99]
	v_mfma_i32_16x16x64_i8 v[92:95], v[148:151], v[206:209], v[92:95]
	v_mfma_i32_16x16x64_i8 v[88:91], v[178:181], v[206:209], v[88:91]
	v_mfma_i32_16x16x64_i8 v[84:87], v[148:151], v[210:213], v[84:87]
	v_mfma_i32_16x16x64_i8 v[80:83], v[178:181], v[210:213], v[80:83]
	v_mfma_i32_16x16x64_i8 v[64:67], v[148:151], v[190:193], v[64:67]
	v_mfma_i32_16x16x64_i8 v[68:71], v[178:181], v[190:193], v[68:71]
	v_mfma_i32_16x16x64_i8 v[72:75], v[148:151], v[194:197], v[72:75]
	v_mfma_i32_16x16x64_i8 v[76:79], v[178:181], v[194:197], v[76:79]
	s_setprio 0
	s_barrier
; #define PG8_STAGE(bufoff, gbase, voff) do { _Pragma("unroll") for (int _i = 0; _i < 2; ++_i) \
;         __builtin_amdgcn_raw_ptr_buffer_load_lds(rsrc, (LAS void*)(lds + (bufoff) + ldsw + _i * 8192), 16, (int)(voff)[_i], (int)(gbase), 0, 0); } while (0)
; #define PG8_STAGE_A(bufoff, h, goff) do { if constexpr (GATHER) { PG8_STAGE(bufoff, goff, vG[h]); } else { PG8_STAGE(bufoff, (goff) + (h) * hstep, voffA); } } while (0)
; #define PG8_WAIT_V(n) asm volatile("s_waitcnt vmcnt(" #n ")" ::: "memory")
; #define PG8_WAIT_L(n) asm volatile("s_waitcnt lgkmcnt(" #n ")" ::: "memory")
; #define PG8_BAR __builtin_amdgcn_s_barrier()
; #define PG8_SCHED __builtin_amdgcn_sched_barrier(0)
;     ...
;             PG8_LDB(B0, 1, 0); PG8_LDB(B1, 1, 1); PG8_SCHED; PG8_LDA(At, 1, 0); PG8_STAGE_A(PG8_SA(0, 1), 1, a2);
;             PG8_WAIT_V(8); PG8_WAIT_L(0); PG8_BAR; PG8_MMA(0, 0, At, B0); PG8_MMA(0, 1, At, B1); PG8_BAR; PG8_SCHED;
;             PG8_LDA(At, 1, 1); PG8_STAGE(PG8_SB(1, 0), b3, voffB); PG8_STAGE(PG8_SB(1, 1), b3 + hstep, voffB); PG8_STAGE_A(PG8_SA(1, 0), 0, a3);
;             PG8_WAIT_V(8); PG8_WAIT_L(0); PG8_BAR; PG8_MMA(1, 0, At, B0); PG8_MMA(1, 1, At, B1); PG8_BAR; PG8_SCHED;
	s_add_i32 s54, 0, 0x18000
	v_add_u32_e32 v96, s54, v157
	v_add_u32_e32 v100, s54, v158
	s_add_i32 s54, 0, 0x1c000
	v_add_u32_e32 v144, s54, v157
	v_add_u32_e32 v148, s54, v158
	ds_read_b128 v[96:99], v96
	ds_read_b128 v[100:103], v100
	ds_read_b128 v[104:107], v169
	ds_read_b128 v[108:111], v170
	ds_read_b128 v[144:147], v144
	ds_read_b128 v[148:151], v148
	ds_read_b128 v[174:177], v171
	ds_read_b128 v[178:181], v172
	s_add_i32 s53, s53, 0x40000
	s_mov_b32 m0, s62
	ds_read_b128 v[182:185], v167 offset:32768
	ds_read_b128 v[186:189], v167 offset:34816
	ds_read_b128 v[190:193], v168 offset:32768
	ds_read_b128 v[194:197], v168 offset:34816
	ds_read_b128 v[198:201], v167 offset:36864
	ds_read_b128 v[202:205], v167 offset:38912
	ds_read_b128 v[206:209], v168 offset:36864
	ds_read_b128 v[210:213], v168 offset:38912
	buffer_load_dwordx4 v153, s[4:7], s53 offen lds
	s_mov_b32 m0, s63
	s_nop 0
	buffer_load_dwordx4 v155, s[4:7], s53 offen lds
	s_waitcnt vmcnt(8)
	s_waitcnt lgkmcnt(0)
	s_barrier
	s_setprio 1
	s_waitcnt lgkmcnt(7)
	v_mfma_i32_16x16x64_i8 v[60:63], v[96:99], v[182:185], v[60:63]
	v_mfma_i32_16x16x64_i8 v[56:59], v[104:107], v[182:185], v[56:59]
	s_waitcnt lgkmcnt(6)
	v_mfma_i32_16x16x64_i8 v[52:55], v[96:99], v[186:189], v[52:55]
	v_mfma_i32_16x16x64_i8 v[48:51], v[104:107], v[186:189], v[48:51]
	s_waitcnt lgkmcnt(3)
	v_mfma_i32_16x16x64_i8 v[44:47], v[96:99], v[198:201], v[44:47]
	v_mfma_i32_16x16x64_i8 v[40:43], v[104:107], v[198:201], v[40:43]
	s_waitcnt lgkmcnt(2)
	v_mfma_i32_16x16x64_i8 v[36:39], v[96:99], v[202:205], v[36:39]
	v_mfma_i32_16x16x64_i8 v[32:35], v[104:107], v[202:205], v[32:35]
	v_mfma_i32_16x16x64_i8 v[60:63], v[100:103], v[190:193], v[60:63]
	v_mfma_i32_16x16x64_i8 v[56:59], v[108:111], v[190:193], v[56:59]
	v_mfma_i32_16x16x64_i8 v[52:55], v[100:103], v[194:197], v[52:55]
	v_mfma_i32_16x16x64_i8 v[48:51], v[108:111], v[194:197], v[48:51]
	s_waitcnt lgkmcnt(1)
	v_mfma_i32_16x16x64_i8 v[44:47], v[100:103], v[206:209], v[44:47]
	v_mfma_i32_16x16x64_i8 v[40:43], v[108:111], v[206:209], v[40:43]
	s_waitcnt lgkmcnt(0)
	v_mfma_i32_16x16x64_i8 v[36:39], v[100:103], v[210:213], v[36:39]
	v_mfma_i32_16x16x64_i8 v[32:35], v[108:111], v[210:213], v[32:35]
	s_setprio 0
	s_setprio 1
	v_mfma_i32_16x16x64_i8 v[140:143], v[144:147], v[182:185], v[140:143]
	v_mfma_i32_16x16x64_i8 v[136:139], v[174:177], v[182:185], v[136:139]
	v_mfma_i32_16x16x64_i8 v[132:135], v[144:147], v[186:189], v[132:135]
	v_mfma_i32_16x16x64_i8 v[128:131], v[174:177], v[186:189], v[128:131]
	v_mfma_i32_16x16x64_i8 v[124:127], v[144:147], v[198:201], v[124:127]
	v_mfma_i32_16x16x64_i8 v[120:123], v[174:177], v[198:201], v[120:123]
	v_mfma_i32_16x16x64_i8 v[116:119], v[144:147], v[202:205], v[116:119]
	v_mfma_i32_16x16x64_i8 v[112:115], v[174:177], v[202:205], v[112:115]
	v_mfma_i32_16x16x64_i8 v[140:143], v[148:151], v[190:193], v[140:143]
	v_mfma_i32_16x16x64_i8 v[136:139], v[178:181], v[190:193], v[136:139]
	v_mfma_i32_16x16x64_i8 v[132:135], v[148:151], v[194:197], v[132:135]
	v_mfma_i32_16x16x64_i8 v[128:131], v[178:181], v[194:197], v[128:131]
	v_mfma_i32_16x16x64_i8 v[124:127], v[148:151], v[206:209], v[124:127]
	v_mfma_i32_16x16x64_i8 v[120:123], v[178:181], v[206:209], v[120:123]
	v_mfma_i32_16x16x64_i8 v[116:119], v[148:151], v[210:213], v[116:119]
	v_mfma_i32_16x16x64_i8 v[112:115], v[178:181], v[210:213], v[112:115]
	s_setprio 0
	s_barrier
	s_mov_b32 m0, s68
	s_add_i32 s53, s51, 0x80
	ds_read_b128 v[182:185], v167 offset:49152
	ds_read_b128 v[186:189], v167 offset:51200
	ds_read_b128 v[190:193], v168 offset:49152
	ds_read_b128 v[194:197], v168 offset:51200
	ds_read_b128 v[198:201], v167 offset:53248
	ds_read_b128 v[202:205], v167 offset:55296
	ds_read_b128 v[206:209], v168 offset:53248
	ds_read_b128 v[210:213], v168 offset:55296
	buffer_load_dwordx4 v154, s[4:7], s53 offen lds
	s_mov_b32 m0, s69
	s_add_i32 s51, s51, 0x40080
	buffer_load_dwordx4 v156, s[4:7], s53 offen lds
	s_mov_b32 m0, s72
	s_nop 0
	buffer_load_dwordx4 v154, s[4:7], s51 offen lds
	s_mov_b32 m0, s73
	s_nop 0
	buffer_load_dwordx4 v156, s[4:7], s51 offen lds
	s_mov_b32 m0, s70
	s_nop 0
	buffer_load_dwordx4 v153, s[4:7], s50 offen lds
	s_mov_b32 m0, s71
	s_nop 0
	buffer_load_dwordx4 v155, s[4:7], s50 offen lds
	s_waitcnt vmcnt(8)
	s_waitcnt lgkmcnt(0)
	s_barrier
	s_setprio 1
	s_waitcnt lgkmcnt(7)
	v_mfma_i32_16x16x64_i8 v[28:31], v[96:99], v[182:185], v[28:31]
	v_mfma_i32_16x16x64_i8 v[24:27], v[104:107], v[182:185], v[24:27]
	s_waitcnt lgkmcnt(6)
	v_mfma_i32_16x16x64_i8 v[20:23], v[96:99], v[186:189], v[20:23]
	v_mfma_i32_16x16x64_i8 v[16:19], v[104:107], v[186:189], v[16:19]
	s_waitcnt lgkmcnt(3)
	v_mfma_i32_16x16x64_i8 v[12:15], v[96:99], v[198:201], v[12:15]
	v_mfma_i32_16x16x64_i8 v[8:11], v[104:107], v[198:201], v[8:11]
	s_waitcnt lgkmcnt(2)
	v_mfma_i32_16x16x64_i8 v[4:7], v[96:99], v[202:205], v[4:7]
	v_mfma_i32_16x16x64_i8 v[0:3], v[104:107], v[202:205], v[0:3]
	v_mfma_i32_16x16x64_i8 v[28:31], v[100:103], v[190:193], v[28:31]
	v_mfma_i32_16x16x64_i8 v[24:27], v[108:111], v[190:193], v[24:27]
	v_mfma_i32_16x16x64_i8 v[20:23], v[100:103], v[194:197], v[20:23]
	v_mfma_i32_16x16x64_i8 v[16:19], v[108:111], v[194:197], v[16:19]
	s_waitcnt lgkmcnt(1)
	v_mfma_i32_16x16x64_i8 v[12:15], v[100:103], v[206:209], v[12:15]
	v_mfma_i32_16x16x64_i8 v[8:11], v[108:111], v[206:209], v[8:11]
	s_waitcnt lgkmcnt(0)
	v_mfma_i32_16x16x64_i8 v[4:7], v[100:103], v[210:213], v[4:7]
	v_mfma_i32_16x16x64_i8 v[0:3], v[108:111], v[210:213], v[0:3]
	s_setprio 0
	s_setprio 1
	v_mfma_i32_16x16x64_i8 v[64:67], v[144:147], v[182:185], v[64:67]
	v_mfma_i32_16x16x64_i8 v[108:111], v[148:151], v[190:193], v[64:67]
	v_mfma_i32_16x16x64_i8 v[64:67], v[174:177], v[182:185], v[68:71]
	v_mfma_i32_16x16x64_i8 v[104:107], v[178:181], v[190:193], v[64:67]
	v_mfma_i32_16x16x64_i8 v[64:67], v[144:147], v[186:189], v[72:75]
	v_mfma_i32_16x16x64_i8 v[100:103], v[148:151], v[194:197], v[64:67]
	v_mfma_i32_16x16x64_i8 v[64:67], v[174:177], v[186:189], v[76:79]
	v_mfma_i32_16x16x64_i8 v[96:99], v[178:181], v[194:197], v[64:67]
	v_mfma_i32_16x16x64_i8 v[64:67], v[144:147], v[198:201], v[92:95]
	v_mfma_i32_16x16x64_i8 v[92:95], v[148:151], v[206:209], v[64:67]
	v_mfma_i32_16x16x64_i8 v[64:67], v[174:177], v[198:201], v[88:91]
	v_mfma_i32_16x16x64_i8 v[88:91], v[178:181], v[206:209], v[64:67]
	v_mfma_i32_16x16x64_i8 v[64:67], v[144:147], v[202:205], v[84:87]
	v_mfma_i32_16x16x64_i8 v[84:87], v[148:151], v[210:213], v[64:67]
	v_mfma_i32_16x16x64_i8 v[64:67], v[174:177], v[202:205], v[80:83]
	v_mfma_i32_16x16x64_i8 v[80:83], v[178:181], v[210:213], v[64:67]
	s_setprio 0
	s_barrier
	s_add_i32 s10, s10, 2
	s_addk_i32 s2, 0x100
	s_addk_i32 s3, 0x100
	s_cmp_gt_u32 s10, 13
	s_cbranch_scc0 .LBB0_337
	s_and_b64 vcc, exec, s[12:13]
	s_cbranch_vccz .LBB0_340
	s_barrier

; #define PG8_STAGE(bufoff, gbase, voff) do { _Pragma("unroll") for (int _i = 0; _i < 2; ++_i) \
;         __builtin_amdgcn_raw_ptr_buffer_load_lds(rsrc, (LAS void*)(lds + (bufoff) + ldsw + _i * 8192), 16, (int)(voff)[_i], (int)(gbase), 0, 0); } while (0)
; #define PG8_STAGE_A(bufoff, h, goff) do { if constexpr (GATHER) { PG8_STAGE(bufoff, goff, vG[h]); } else { PG8_STAGE(bufoff, (goff) + (h) * hstep, voffA); } } while (0)
; #define PG8_WAIT_V(n) asm volatile("s_waitcnt vmcnt(" #n ")" ::: "memory")
; #define PG8_WAIT_L(n) asm volatile("s_waitcnt lgkmcnt(" #n ")" ::: "memory")
; #define PG8_BAR __builtin_amdgcn_s_barrier()
; #define PG8_SCHED __builtin_amdgcn_sched_barrier(0)
;     DI int row_cnt(const pg8::Unit& u) const { return __builtin_amdgcn_readfirstlane(tab[u.a0]) - u.ldc; }
;     ...
;         for (int t = 0; t < nt; t += 2) {
;             const bool last = (t == nt - 2);
;             const unsigned a1 = cA + (unsigned)(t + 1) * kstep;
;             const unsigned a2 = last ? nA : cA + (unsigned)(t + 2) * kstep, b2 = last ? nB : cB + (unsigned)(t + 2) * kstep;
;             const unsigned a3 = a2 + kstep, b3 = b2 + kstep;
;             if constexpr (SP2) {
;             PG8_LDB(B0, 0, 0); PG8_LDB(B1, 0, 1); PG8_SCHED; PG8_LDA(At, 0, 0); PG8_STAGE_A(PG8_SA(1, 1), 1, a1);
;             if constexpr (GATHER) { if (last && has_next) load_rows((ui + 1) & 1, S.row_cnt(nxt)); }
;             PG8_WAIT_V(8); PG8_WAIT_L(0); PG8_BAR; PG8_MMA(0, 0, At, B0); PG8_MMA(0, 1, At, B1); PG8_BAR; PG8_SCHED;
;             PG8_LDA(At, 0, 1); PG8_STAGE(PG8_SB(0, 0), b2, voffB); PG8_STAGE(PG8_SB(0, 1), b2 + hstep, voffB); PG8_STAGE_A(PG8_SA(0, 0), 0, a2);
;             PG8_WAIT_V(8); PG8_WAIT_L(0); PG8_BAR; PG8_MMA(1, 0, At, B0); PG8_MMA(1, 1, At, B1); PG8_BAR; PG8_SCHED;
.LBB0_1335:
	ds_read_b128 v[128:131], v152
	ds_read_b128 v[136:139], v152 offset:2048
	ds_read_b128 v[132:135], v153
	ds_read_b128 v[140:143], v153 offset:2048
	ds_read_b128 v[158:161], v154
	ds_read_b128 v[166:169], v154 offset:2048
	ds_read_b128 v[162:165], v155
	ds_read_b128 v[170:173], v155 offset:2048
	s_add_i32 s4, s3, 0xfffc0080
	s_cmp_eq_u32 s54, 12
	s_cselect_b32 s57, s52, s4
	s_cselect_b32 s56, s51, s53
	s_add_i32 s55, s57, 0x80
	s_mov_b32 s4, s62
	s_mov_b32 m0, s41
	ds_read_b128 v[174:177], v156
	ds_read_b128 v[182:185], v156 offset:2048
	ds_read_b128 v[178:181], v157
	ds_read_b128 v[186:189], v157 offset:2048
	ds_read_b128 v[190:193], v156 offset:4096
	ds_read_b128 v[198:201], v156 offset:6144
	ds_read_b128 v[194:197], v157 offset:4096
	ds_read_b128 v[202:205], v157 offset:6144
	buffer_load_dwordx4 v146, s[4:7], s3 offen lds
	s_mov_b32 m0, s44
	s_nop 0
	buffer_load_dwordx4 v148, s[4:7], s3 offen lds
	s_waitcnt vmcnt(8)
	s_waitcnt lgkmcnt(0)
	s_barrier
	s_setprio 1
	s_waitcnt lgkmcnt(5)
	v_mfma_f32_16x16x128_f8f6f4 v[124:127], v[128:135], v[174:181], v[124:127]
	v_mfma_f32_16x16x128_f8f6f4 v[120:123], v[136:143], v[174:181], v[120:123]
	s_waitcnt lgkmcnt(4)
	v_mfma_f32_16x16x128_f8f6f4 v[108:111], v[128:135], v[182:189], v[108:111]
	v_mfma_f32_16x16x128_f8f6f4 v[104:107], v[136:143], v[182:189], v[104:107]
	s_waitcnt lgkmcnt(1)
	v_mfma_f32_16x16x128_f8f6f4 v[206:209], v[128:135], v[190:197], v[92:95]
	v_mfma_f32_16x16x128_f8f6f4 v[210:213], v[136:143], v[190:197], v[88:91]
	s_waitcnt lgkmcnt(0)
	v_mfma_f32_16x16x128_f8f6f4 v[214:217], v[128:135], v[198:205], v[76:79]
	v_mfma_f32_16x16x128_f8f6f4 v[218:221], v[136:143], v[198:205], v[72:75]
	s_setprio 0
	s_setprio 1
	v_mfma_f32_16x16x128_f8f6f4 v[116:119], v[158:165], v[174:181], v[116:119]
	v_mfma_f32_16x16x128_f8f6f4 v[112:115], v[166:173], v[174:181], v[112:115]
	v_mfma_f32_16x16x128_f8f6f4 v[100:103], v[158:165], v[182:189], v[100:103]
	v_mfma_f32_16x16x128_f8f6f4 v[96:99], v[166:173], v[182:189], v[96:99]
	v_mfma_f32_16x16x128_f8f6f4 v[174:177], v[158:165], v[190:197], v[84:87]
	v_mfma_f32_16x16x128_f8f6f4 v[178:181], v[166:173], v[190:197], v[80:83]
	v_mfma_f32_16x16x128_f8f6f4 v[182:185], v[158:165], v[198:205], v[68:71]
	v_mfma_f32_16x16x128_f8f6f4 v[186:189], v[166:173], v[198:205], v[64:67]
	s_setprio 0
	s_barrier
	s_mov_b32 m0, s24
	s_nop 3
	ds_read_b128 v[64:67], v156 offset:16384
	ds_read_b128 v[72:75], v156 offset:18432
	ds_read_b128 v[68:71], v157 offset:16384
	ds_read_b128 v[76:79], v157 offset:18432
	ds_read_b128 v[80:83], v156 offset:20480
	ds_read_b128 v[88:91], v156 offset:22528
	ds_read_b128 v[84:87], v157 offset:20480
	ds_read_b128 v[92:95], v157 offset:22528
	buffer_load_dwordx4 v147, s[4:7], s56 offen lds
	s_mov_b32 m0, s25
	s_add_i32 s58, s56, 0x4000
	buffer_load_dwordx4 v149, s[4:7], s56 offen lds
	s_mov_b32 m0, s26
	s_nop 0
	buffer_load_dwordx4 v147, s[4:7], s58 offen lds
	s_mov_b32 m0, s27
	s_nop 0
	buffer_load_dwordx4 v149, s[4:7], s58 offen lds
	s_mov_b32 m0, s17
	s_nop 0
	buffer_load_dwordx4 v146, s[4:7], s57 offen lds
	s_mov_b32 m0, s28
	s_nop 0
	buffer_load_dwordx4 v148, s[4:7], s57 offen lds
	s_waitcnt vmcnt(8)
	s_waitcnt lgkmcnt(0)
	s_barrier
	s_setprio 1
	s_waitcnt lgkmcnt(5)
	v_mfma_f32_16x16x128_f8f6f4 v[60:63], v[128:135], v[64:71], v[60:63]
	v_mfma_f32_16x16x128_f8f6f4 v[56:59], v[136:143], v[64:71], v[56:59]
	s_waitcnt lgkmcnt(4)
	v_mfma_f32_16x16x128_f8f6f4 v[190:193], v[128:135], v[72:79], v[44:47]
	v_mfma_f32_16x16x128_f8f6f4 v[194:197], v[136:143], v[72:79], v[40:43]
	s_waitcnt lgkmcnt(1)
	v_mfma_f32_16x16x128_f8f6f4 v[198:201], v[128:135], v[80:87], v[28:31]
	v_mfma_f32_16x16x128_f8f6f4 v[202:205], v[136:143], v[80:87], v[24:27]
	s_waitcnt lgkmcnt(0)
	v_mfma_f32_16x16x128_f8f6f4 v[222:225], v[128:135], v[88:95], v[12:15]
	v_mfma_f32_16x16x128_f8f6f4 v[226:229], v[136:143], v[88:95], v[8:11]
	s_setprio 0
	s_setprio 1
	v_mfma_f32_16x16x128_f8f6f4 v[52:55], v[158:165], v[64:71], v[52:55]
	v_mfma_f32_16x16x128_f8f6f4 v[48:51], v[166:173], v[64:71], v[48:51]
	v_mfma_f32_16x16x128_f8f6f4 v[230:233], v[158:165], v[72:79], v[36:39]
	v_mfma_f32_16x16x128_f8f6f4 v[234:237], v[166:173], v[72:79], v[32:35]
	v_mfma_f32_16x16x128_f8f6f4 v[238:241], v[158:165], v[80:87], v[20:23]
	v_mfma_f32_16x16x128_f8f6f4 v[242:245], v[166:173], v[80:87], v[16:19]
	v_mfma_f32_16x16x128_f8f6f4 v[246:249], v[158:165], v[88:95], v[4:7]
	v_mfma_f32_16x16x128_f8f6f4 v[250:253], v[166:173], v[88:95], v[0:3]
	s_setprio 0
	s_barrier
; #define PG8_STAGE(bufoff, gbase, voff) do { _Pragma("unroll") for (int _i = 0; _i < 2; ++_i) \
;         __builtin_amdgcn_raw_ptr_buffer_load_lds(rsrc, (LAS void*)(lds + (bufoff) + ldsw + _i * 8192), 16, (int)(voff)[_i], (int)(gbase), 0, 0); } while (0)
; #define PG8_STAGE_A(bufoff, h, goff) do { if constexpr (GATHER) { PG8_STAGE(bufoff, goff, vG[h]); } else { PG8_STAGE(bufoff, (goff) + (h) * hstep, voffA); } } while (0)
; #define PG8_WAIT_V(n) asm volatile("s_waitcnt vmcnt(" #n ")" ::: "memory")
; #define PG8_WAIT_L(n) asm volatile("s_waitcnt lgkmcnt(" #n ")" ::: "memory")
; #define PG8_BAR __builtin_amdgcn_s_barrier()
; #define PG8_SCHED __builtin_amdgcn_sched_barrier(0)
;     ...
;             PG8_LDB(B0, 1, 0); PG8_LDB(B1, 1, 1); PG8_SCHED; PG8_LDA(At, 1, 0); PG8_STAGE_A(PG8_SA(0, 1), 1, a2);
;             PG8_WAIT_V(8); PG8_WAIT_L(0); PG8_BAR; PG8_MMA(0, 0, At, B0); PG8_MMA(0, 1, At, B1); PG8_BAR; PG8_SCHED;
;             PG8_LDA(At, 1, 1); PG8_STAGE(PG8_SB(1, 0), b3, voffB); PG8_STAGE(PG8_SB(1, 1), b3 + hstep, voffB); PG8_STAGE_A(PG8_SA(1, 0), 0, a3);
;             PG8_WAIT_V(8); PG8_WAIT_L(0); PG8_BAR; PG8_MMA(1, 0, At, B0); PG8_MMA(1, 1, At, B1); PG8_BAR; PG8_SCHED;
;     ...
;         if constexpr (ALIGN_EPI) { if (wr == 0) PG8_BAR; }
	s_add_i32 s58, 0, 0x18000
	s_nop 2
	v_add_u32_e32 v4, s58, v150
	v_add_u32_e32 v8, s58, v151
	s_add_i32 s58, 0, 0x1c000
	ds_read_b128 v[0:3], v4
	ds_read_b128 v[16:19], v4 offset:2048
	ds_read_b128 v[4:7], v8
	ds_read_b128 v[20:23], v8 offset:2048
	v_add_u32_e32 v8, s58, v150
	v_add_u32_e32 v9, s58, v151
	ds_read_b128 v[128:131], v8
	ds_read_b128 v[136:139], v8 offset:2048
	ds_read_b128 v[132:135], v9
	ds_read_b128 v[140:143], v9 offset:2048
	s_add_i32 s57, s57, 0x40000
	s_mov_b32 m0, s29
	ds_read_b128 v[8:11], v156 offset:32768
	ds_read_b128 v[24:27], v156 offset:34816
	ds_read_b128 v[12:15], v157 offset:32768
	ds_read_b128 v[28:31], v157 offset:34816
	ds_read_b128 v[32:35], v156 offset:36864
	ds_read_b128 v[40:43], v156 offset:38912
	ds_read_b128 v[36:39], v157 offset:36864
	ds_read_b128 v[44:47], v157 offset:38912
	buffer_load_dwordx4 v146, s[4:7], s57 offen lds
	s_mov_b32 m0, s31
	s_nop 0
	buffer_load_dwordx4 v148, s[4:7], s57 offen lds
	s_waitcnt vmcnt(8)
	s_waitcnt lgkmcnt(0)
	s_barrier
	s_setprio 1
	s_waitcnt lgkmcnt(5)
	v_mfma_f32_16x16x128_f8f6f4 v[124:127], v[0:7], v[8:15], v[124:127]
	v_mfma_f32_16x16x128_f8f6f4 v[120:123], v[16:23], v[8:15], v[120:123]
	s_waitcnt lgkmcnt(4)
	v_mfma_f32_16x16x128_f8f6f4 v[108:111], v[0:7], v[24:31], v[108:111]
	v_mfma_f32_16x16x128_f8f6f4 v[104:107], v[16:23], v[24:31], v[104:107]
	s_waitcnt lgkmcnt(1)
	v_mfma_f32_16x16x128_f8f6f4 v[92:95], v[0:7], v[32:39], v[206:209]
	v_mfma_f32_16x16x128_f8f6f4 v[88:91], v[16:23], v[32:39], v[210:213]
	s_waitcnt lgkmcnt(0)
	v_mfma_f32_16x16x128_f8f6f4 v[76:79], v[0:7], v[40:47], v[214:217]
	v_mfma_f32_16x16x128_f8f6f4 v[72:75], v[16:23], v[40:47], v[218:221]
	s_setprio 0
	s_setprio 1
	v_mfma_f32_16x16x128_f8f6f4 v[116:119], v[128:135], v[8:15], v[116:119]
	v_mfma_f32_16x16x128_f8f6f4 v[112:115], v[136:143], v[8:15], v[112:115]
	v_mfma_f32_16x16x128_f8f6f4 v[100:103], v[128:135], v[24:31], v[100:103]
	v_mfma_f32_16x16x128_f8f6f4 v[96:99], v[136:143], v[24:31], v[96:99]
	v_mfma_f32_16x16x128_f8f6f4 v[84:87], v[128:135], v[32:39], v[174:177]
	v_mfma_f32_16x16x128_f8f6f4 v[80:83], v[136:143], v[32:39], v[178:181]
	v_mfma_f32_16x16x128_f8f6f4 v[68:71], v[128:135], v[40:47], v[182:185]
	v_mfma_f32_16x16x128_f8f6f4 v[64:67], v[136:143], v[40:47], v[186:189]
	s_setprio 0
	s_barrier
	s_mov_b32 m0, s33
	s_add_i32 s57, s56, 0x80
	ds_read_b128 v[32:35], v156 offset:49152
	ds_read_b128 v[158:161], v156 offset:51200
	ds_read_b128 v[36:39], v157 offset:49152
	ds_read_b128 v[162:165], v157 offset:51200
	ds_read_b128 v[166:169], v156 offset:53248
	ds_read_b128 v[174:177], v156 offset:55296
	ds_read_b128 v[170:173], v157 offset:53248
	ds_read_b128 v[178:181], v157 offset:55296
	buffer_load_dwordx4 v147, s[4:7], s57 offen lds
	s_mov_b32 m0, s34
	s_add_i32 s56, s56, 0x4080
	buffer_load_dwordx4 v149, s[4:7], s57 offen lds
	s_mov_b32 m0, s37
	s_nop 0
	buffer_load_dwordx4 v147, s[4:7], s56 offen lds
	s_mov_b32 m0, s38
	s_nop 0
	buffer_load_dwordx4 v149, s[4:7], s56 offen lds
	s_mov_b32 m0, s35
	s_nop 0
	buffer_load_dwordx4 v146, s[4:7], s55 offen lds
	s_mov_b32 m0, s36
	s_nop 0
	buffer_load_dwordx4 v148, s[4:7], s55 offen lds
	s_waitcnt vmcnt(8)
	s_waitcnt lgkmcnt(0)
	s_barrier
	s_setprio 1
	s_waitcnt lgkmcnt(5)
	v_mfma_f32_16x16x128_f8f6f4 v[60:63], v[0:7], v[32:39], v[60:63]
	v_mfma_f32_16x16x128_f8f6f4 v[56:59], v[16:23], v[32:39], v[56:59]
	s_waitcnt lgkmcnt(4)
	v_mfma_f32_16x16x128_f8f6f4 v[44:47], v[0:7], v[158:165], v[190:193]
	v_mfma_f32_16x16x128_f8f6f4 v[40:43], v[16:23], v[158:165], v[194:197]
	s_waitcnt lgkmcnt(1)
	v_mfma_f32_16x16x128_f8f6f4 v[28:31], v[0:7], v[166:173], v[198:201]
	v_mfma_f32_16x16x128_f8f6f4 v[24:27], v[16:23], v[166:173], v[202:205]
	s_waitcnt lgkmcnt(0)
	v_mfma_f32_16x16x128_f8f6f4 v[12:15], v[0:7], v[174:181], v[222:225]
	v_mfma_f32_16x16x128_f8f6f4 v[8:11], v[16:23], v[174:181], v[226:229]
	s_setprio 0
	s_setprio 1
	v_mfma_f32_16x16x128_f8f6f4 v[52:55], v[128:135], v[32:39], v[52:55]
	v_mfma_f32_16x16x128_f8f6f4 v[48:51], v[136:143], v[32:39], v[48:51]
	v_mfma_f32_16x16x128_f8f6f4 v[36:39], v[128:135], v[158:165], v[230:233]
	v_mfma_f32_16x16x128_f8f6f4 v[32:35], v[136:143], v[158:165], v[234:237]
	v_mfma_f32_16x16x128_f8f6f4 v[20:23], v[128:135], v[166:173], v[238:241]
	v_mfma_f32_16x16x128_f8f6f4 v[16:19], v[136:143], v[166:173], v[242:245]
	v_mfma_f32_16x16x128_f8f6f4 v[4:7], v[128:135], v[174:181], v[246:249]
	v_mfma_f32_16x16x128_f8f6f4 v[0:3], v[136:143], v[174:181], v[250:253]
	s_setprio 0
	s_barrier
	s_add_i32 s54, s54, 2
	s_addk_i32 s3, 0x100
	s_addk_i32 s53, 0x100
	s_cmp_gt_u32 s54, 13
	s_cbranch_scc0 .LBB0_1335
	s_and_b64 vcc, exec, s[14:15]
	s_cbranch_vccz .LBB0_1338
	s_barrier
